# MoE: expert counters, first-unit and per-unit slot-list loads issued as batches instead of serialized vmcnt(0) round trips; down-GEMM next-unit offsets rebuilt from raw slots each K iteration
# speedup vs baseline: 1.0243x; 1.0159x over previous
; #define LAS __attribute__((address_space(3)))
; template <int PH, bool PRB = false>
; __device__ __forceinline__ void run_phase(int layer, LAS unsigned char* lds, const int wv_) {
;     ...
;     if constexpr (PH == PH_MOE) {
;         LAS int* moe = (LAS int*)(lds + LDS_MOE);
;         if (tid == 0) { int acc = 0; for (int e = 0; e < 16; ++e) { const int c = (int)ctl[CW_CNT + (layer * 16 + e) * 64]; moe[e] = acc; moe[17 + e] = c; acc += (c + 255) >> 8; } moe[16] = acc; }
;         __syncthreads();
.LBB0_1585:
	s_mov_b64 s[0:1], 0
	s_mov_b32 s5, s80
	s_waitcnt lgkmcnt(0)
	s_barrier
	v_readlane_b32 s2, v254, 1
	v_readlane_b32 s3, v254, 2
	s_add_u32 s0, s2, s0
	s_addc_u32 s1, s3, s1
	s_load_dwordx2 s[8:9], s[0:1], 0xe0
	v_mbcnt_lo_u32_b32 v0, -1, 0
	v_mbcnt_hi_u32_b32 v0, -1, v0
	v_readlane_b32 s36, v254, 0
	v_add_u32_e32 v0, s93, v0
	s_nop 0
	v_cmp_eq_u32_e32 vcc, 0, v0
	s_and_saveexec_b64 s[0:1], vcc
	s_cbranch_execz .LBB0_1587
	s_lshl_b32 s2, s5, 10
	s_ashr_i32 s3, s2, 31
	s_lshl_b64 s[2:3], s[2:3], 2
	s_waitcnt lgkmcnt(0)
	s_add_u32 s2, s8, s2
	s_addc_u32 s3, s9, s3
	v_mov_b32_e32 v12, 0x1000
	global_load_dword v16, v12, s[2:3]
	global_load_dword v17, v12, s[2:3] offset:256
	global_load_dword v18, v12, s[2:3] offset:512
	global_load_dword v19, v12, s[2:3] offset:768
	global_load_dword v20, v12, s[2:3] offset:1024
	global_load_dword v21, v12, s[2:3] offset:1280
	global_load_dword v22, v12, s[2:3] offset:1536
	global_load_dword v23, v12, s[2:3] offset:1792
	global_load_dword v24, v12, s[2:3] offset:2048
	global_load_dword v25, v12, s[2:3] offset:2304
	global_load_dword v26, v12, s[2:3] offset:2560
	global_load_dword v27, v12, s[2:3] offset:2816
	global_load_dword v28, v12, s[2:3] offset:3072
	global_load_dword v29, v12, s[2:3] offset:3328
	global_load_dword v30, v12, s[2:3] offset:3584
	global_load_dword v31, v12, s[2:3] offset:3840
	s_waitcnt vmcnt(0)
	v_mov_b32_e32 v1, v16
	v_mov_b32_e32 v2, v17
	v_mov_b32_e32 v3, v18
	v_mov_b32_e32 v8, v19
	v_mov_b32_e32 v9, v20
	v_mov_b32_e32 v10, v21
	v_mov_b32_e32 v11, v22
	v_readlane_b32 s4, v254, 29
	v_mov_b32_e32 v4, v65
	s_waitcnt vmcnt(6)
	v_add_u32_e32 v0, 0xff, v1
	v_ashrrev_i32_e32 v5, 8, v0
	s_waitcnt vmcnt(5)
	v_add_u32_e32 v0, 0xff, v2
	v_ashrrev_i32_e32 v0, 8, v0
	v_add_u32_e32 v6, v0, v5
	s_waitcnt vmcnt(4)
	v_add_u32_e32 v0, 0xff, v3
	v_ashrrev_i32_e32 v0, 8, v0
	v_add_u32_e32 v7, v0, v6
	v_mov_b32_e32 v0, s4
	ds_write_b128 v0, v[4:7]
	s_waitcnt vmcnt(3)
	v_add_u32_e32 v0, 0xff, v8
	v_ashrrev_i32_e32 v0, 8, v0
	v_add_u32_e32 v4, v0, v7
	s_waitcnt vmcnt(2)
	v_add_u32_e32 v0, 0xff, v9
	v_ashrrev_i32_e32 v0, 8, v0
	v_add_u32_e32 v5, v0, v4
	s_waitcnt vmcnt(1)
	v_add_u32_e32 v0, 0xff, v10
	v_ashrrev_i32_e32 v0, 8, v0
	v_readlane_b32 s4, v254, 30
	v_add_u32_e32 v6, v0, v5
	s_nop 0
	v_mov_b32_e32 v0, s4
	s_waitcnt vmcnt(0)
	ds_write_b128 v0, v[8:11]
	s_nop 1
	v_mov_b32_e32 v8, v23
	v_mov_b32_e32 v9, v24
	v_mov_b32_e32 v10, v25
	v_add_u32_e32 v0, 0xff, v11
	v_mov_b32_e32 v11, v26
	v_ashrrev_i32_e32 v0, 8, v0
	v_readlane_b32 s4, v254, 31
	v_add_u32_e32 v7, v0, v6
	s_nop 0
	v_mov_b32_e32 v0, s4
	ds_write_b128 v0, v[4:7]
	v_readlane_b32 s4, v254, 32
	s_waitcnt vmcnt(3)
	v_add_u32_e32 v0, 0xff, v8
	v_ashrrev_i32_e32 v0, 8, v0
	v_add_u32_e32 v4, v0, v7
	s_waitcnt vmcnt(2)
	v_add_u32_e32 v0, 0xff, v9
	v_ashrrev_i32_e32 v0, 8, v0
	v_add_u32_e32 v5, v0, v4
	s_waitcnt vmcnt(1)
	v_add_u32_e32 v0, 0xff, v10
	v_ashrrev_i32_e32 v0, 8, v0
	v_add_u32_e32 v6, v0, v5
	v_mov_b32_e32 v0, s4
	s_waitcnt vmcnt(0)
	ds_write_b128 v0, v[8:11]
	s_nop 1
	v_mov_b32_e32 v8, v27
	v_mov_b32_e32 v9, v28
	v_mov_b32_e32 v10, v29
	v_add_u32_e32 v0, 0xff, v11
	v_mov_b32_e32 v11, v30
	v_ashrrev_i32_e32 v0, 8, v0
	v_readlane_b32 s4, v254, 33
	v_add_u32_e32 v7, v0, v6
	s_nop 0
	v_mov_b32_e32 v0, s4
	ds_write_b128 v0, v[4:7]
	v_readlane_b32 s4, v254, 34
	s_waitcnt vmcnt(3)
	v_add_u32_e32 v0, 0xff, v8
	v_ashrrev_i32_e32 v0, 8, v0
	v_add_u32_e32 v4, v0, v7
	s_waitcnt vmcnt(2)
	v_add_u32_e32 v0, 0xff, v9
	v_ashrrev_i32_e32 v0, 8, v0
	v_add_u32_e32 v5, v0, v4
	s_waitcnt vmcnt(1)
	v_add_u32_e32 v0, 0xff, v10
	v_ashrrev_i32_e32 v0, 8, v0
	v_add_u32_e32 v6, v0, v5
	v_mov_b32_e32 v0, s4
	s_waitcnt vmcnt(0)
	ds_write_b128 v0, v[8:11]
	v_add_u32_e32 v0, 0xff, v11
	v_ashrrev_i32_e32 v0, 8, v0
	v_add_u32_e32 v7, v0, v6
	v_mov_b32_e32 v0, v31
	v_readlane_b32 s2, v254, 35
	s_nop 1
	v_mov_b32_e32 v8, s2
	v_readlane_b32 s2, v254, 36
	ds_write_b128 v8, v[4:7]
	s_nop 0
	v_mov_b32_e32 v4, s2
	v_readlane_b32 s2, v254, 37
	s_waitcnt vmcnt(0)
	ds_write_b32 v4, v0
	v_add_u32_e32 v0, 0xff, v0
	v_ashrrev_i32_e32 v0, 8, v0
	v_add_u32_e32 v0, v0, v7
	v_mov_b32_e32 v4, s2
	ds_write_b128 v4, v[0:3]

;     __device__ __forceinline__ unsigned arow(const Unit& u, int r) const { return (unsigned)(((hot & 1) ? 0 : u.pm * BM) + r) * (unsigned)(K * 2); }
;     __device__ __forceinline__ unsigned arow(const Unit& u, int r) const {
;         const int idx = r < u.rows ? r : u.rows - 1; const int slot = list[u.e * LCAP + u.pm * BM + idx];
;         return (unsigned)(TOKEN_ROWS ? (slot >> 1) : slot) * (unsigned)(K * 2);
.LBB0_1590:
	s_add_u32 s10, s8, 0xa100000
	s_addc_u32 s11, s9, 0
	s_add_u32 s12, s8, 0x21900000
	s_mul_i32 s2, s5, 0x2800
	s_addc_u32 s13, s9, 0
	s_ashr_i32 s3, s2, 31
	s_lshl_b64 s[2:3], s[2:3], 2
	s_add_u32 s2, s8, s2
	s_addc_u32 s3, s9, s3
	s_add_u32 s43, s2, 0x80000
	s_addc_u32 s44, s3, 0
	s_andn2_b64 vcc, exec, s[0:1]
	s_cbranch_vccnz .LBB0_1628
	v_bfe_i32 v3, v0, 27, 1
	v_lshlrev_b32_e32 v1, 4, v0
	v_lshrrev_b32_e32 v3, 22, v3
	v_add_u32_e32 v3, v1, v3
	v_and_b32_e32 v3, 0xfffffc00, v3
	v_sub_u32_e32 v1, v1, v3
	v_ashrrev_i32_e32 v2, 31, v0
	v_lshrrev_b32_e32 v3, 4, v1
	v_lshrrev_b32_e32 v2, 26, v2
	v_bitop3_b32 v3, v3, v1, 32 bitop3:0x6c
	v_ashrrev_i32_e32 v1, 31, v1
	v_add_u32_e32 v2, v0, v2
	v_lshrrev_b32_e32 v1, 26, v1
	v_ashrrev_i32_e32 v2, 6, v2
	v_add_u32_e32 v1, v3, v1
	v_lshlrev_b32_e32 v4, 3, v2
	v_ashrrev_i32_e32 v1, 6, v1
	v_and_b32_e32 v4, -16, v4
	v_mul_i32_i24_e32 v5, 64, v1
	v_add_u32_e32 v4, v1, v4
	v_sub_u32_e32 v3, v3, v5
	v_lshlrev_b32_e32 v2, 5, v2
	v_ashrrev_i16_sdwa v3, v227, sext(v3) dst_sel:DWORD dst_unused:UNUSED_PAD src0_sel:DWORD src1_sel:BYTE_0
	v_lshlrev_b32_e32 v5, 1, v4
	v_lshrrev_b32_e32 v6, 2, v4
	v_and_b32_e32 v1, 3, v1
	s_mov_b32 s0, 0x3fffe0
	v_and_b32_e32 v2, 32, v2
	v_bfe_i32 v3, v3, 0, 16
	v_and_b32_e32 v5, 24, v5
	v_and_b32_e32 v6, 4, v6
	v_and_or_b32 v1, v4, s0, v1
	v_or3_b32 v1, v1, v6, v5
	v_add_lshl_u32 v2, v2, v3, 1
	v_lshl_add_u32 v220, v1, 10, v2
	v_mbcnt_lo_u32_b32 v1, -1, 0
	v_mbcnt_hi_u32_b32 v1, -1, v1
	s_add_u32 s37, s8, 0x1e400000
	v_add_u32_e32 v1, s93, v1
	s_addc_u32 s38, s9, 0
	v_ashrrev_i32_e32 v2, 31, v1
	v_lshrrev_b32_e32 v2, 26, v2
	v_lshlrev_b32_e32 v4, 4, v1
	v_add_u32_e32 v2, v1, v2
	v_bfe_i32 v1, v1, 27, 1
	v_lshrrev_b32_e32 v1, 22, v1
	v_add_u32_e32 v1, v4, v1
	v_and_b32_e32 v1, 0xfffffc00, v1
	v_sub_u32_e32 v1, v4, v1
	v_lshrrev_b32_e32 v3, 4, v1
	v_bitop3_b32 v3, v3, v1, 32 bitop3:0x6c
	v_ashrrev_i32_e32 v1, 31, v1
	v_ashrrev_i32_e32 v2, 6, v2
	v_lshrrev_b32_e32 v1, 26, v1
	v_lshlrev_b32_e32 v5, 3, v2
	v_add_u32_e32 v1, v3, v1
	s_add_u32 s2, s8, 0x3100000
	v_and_b32_e32 v5, -16, v5
	v_ashrrev_i32_e32 v1, 6, v1
	s_addc_u32 s3, s9, 0
	s_add_i32 s0, s40, -1
	s_lshl_b32 s1, s6, 14
	s_lshl_b32 s7, s33, 8
	v_add_u32_e32 v5, v1, v5
	v_lshlrev_b32_e32 v2, 5, v2
	s_add_i32 s1, s1, s7
	v_and_b32_e32 v6, 32, v2
	v_min_i32_e32 v2, s0, v5
	v_mul_i32_i24_e32 v1, 64, v1
	v_add_u32_e32 v2, s1, v2
	v_sub_u32_e32 v1, v3, v1
	v_ashrrev_i32_e32 v3, 31, v2
	v_lshl_add_u64 v[2:3], v[2:3], 2, s[12:13]
	global_load_dword v16, v[2:3], off
	v_ashrrev_i16_sdwa v1, v227, sext(v1) dst_sel:DWORD dst_unused:UNUSED_PAD src0_sel:DWORD src1_sel:BYTE_0
	v_bfe_i32 v1, v1, 0, 16
	v_add_lshl_u32 v20, v6, v1, 1
	s_ashr_i32 s5, s4, 6
	s_ashr_i32 s7, s6, 31
	s_ashr_i32 s29, s28, 31
	s_ashr_i32 s18, s4, 8
	s_lshl_b32 s39, s5, 10
	s_lshl_b64 s[14:15], s[28:29], 18
	v_mov_b32_e32 v64, v220
	v_add_u32_e32 v2, 0x80, v5
	v_min_i32_e32 v2, s0, v2
	v_add_u32_e32 v2, s1, v2
	v_ashrrev_i32_e32 v3, 31, v2
	v_lshl_add_u64 v[2:3], v[2:3], 2, s[12:13]
	global_load_dword v17, v[2:3], off
	v_add_u32_e32 v1, 0x2000, v4
	v_ashrrev_i32_e32 v2, 31, v1
	v_lshrrev_b32_e32 v2, 22, v2
	v_add_u32_e32 v2, v1, v2
	v_ashrrev_i32_e32 v2, 10, v2
	v_mul_i32_i24_e32 v3, 0x400, v2
	v_sub_u32_e32 v1, v1, v3
	v_lshrrev_b32_e32 v3, 4, v1
	v_bitop3_b32 v1, v3, v1, 32 bitop3:0x6c
	v_ashrrev_i32_e32 v4, 31, v1
	v_lshrrev_b32_e32 v4, 26, v4
	v_lshlrev_b32_e32 v3, 3, v2
	v_add_u32_e32 v4, v1, v4
	v_and_b32_e32 v3, -16, v3
	v_ashrrev_i32_e32 v5, 6, v4
	v_lshlrev_b32_e32 v2, 5, v2
	v_add_u32_e32 v5, v5, v3
	v_and_b32_e32 v6, 32, v2
	v_and_b32_e32 v2, 0xc0, v4
	v_sub_u32_e32 v1, v1, v2
	v_min_i32_e32 v2, s0, v5
	v_add_u32_e32 v2, s1, v2
	v_ashrrev_i32_e32 v3, 31, v2
	v_lshl_add_u64 v[2:3], v[2:3], 2, s[12:13]
	global_load_dword v18, v[2:3], off
	v_ashrrev_i16_sdwa v1, v227, sext(v1) dst_sel:DWORD dst_unused:UNUSED_PAD src0_sel:DWORD src1_sel:BYTE_0
	v_bfe_i32 v1, v1, 0, 16
	v_add_lshl_u32 v21, v6, v1, 1
	v_add_u32_e32 v2, 0x80, v5
	v_min_i32_e32 v2, s0, v2
	v_add_u32_e32 v2, s1, v2
	v_ashrrev_i32_e32 v3, 31, v2
	v_lshl_add_u64 v[2:3], v[2:3], 2, s[12:13]
	global_load_dword v19, v[2:3], off
	s_lshl_b64 s[0:1], s[6:7], 20
	s_add_u32 s7, s37, s14
	s_addc_u32 s14, s38, s15
	s_add_u32 s0, s7, s0
	s_addc_u32 s1, s14, s1
	s_add_i32 s29, s39, 0x100
	s_add_i32 m0, s29, 0x10000
	s_add_i32 s41, s29, 0x2000
	global_load_lds_dwordx4 v64, s[0:1]
	s_add_i32 m0, s29, 0x12000
	s_add_i32 s45, s29, 0x4000
	s_add_i32 s48, s29, 0x6000
	v_lshl_add_u64 v[2:3], s[0:1], 0, v[64:65]
	v_lshl_add_u64 v[2:3], v[2:3], 0, s[82:83]
	v_mov_b32_e32 v64, v220
	global_load_lds_dwordx4 v[2:3], off
	s_add_i32 m0, s29, 0x14000
	v_lshl_add_u64 v[2:3], s[0:1], 0, v[64:65]
	v_lshl_add_u64 v[4:5], v[2:3], 0, s[66:67]
	global_load_lds_dwordx4 v[4:5], off
	v_lshl_add_u64 v[2:3], v[2:3], 0, s[84:85]
	s_add_i32 m0, s29, 0x16000
	s_nop 0
	global_load_lds_dwordx4 v[2:3], off
	s_waitcnt vmcnt(4)
	v_lshlrev_b32_e32 v16, 9, v16
	v_lshlrev_b32_e32 v17, 9, v17
	v_lshlrev_b32_e32 v18, 9, v18
	v_lshlrev_b32_e32 v19, 9, v19
	v_and_b32_e32 v16, 0xfffffc00, v16
	v_and_b32_e32 v17, 0xfffffc00, v17
	v_and_b32_e32 v18, 0xfffffc00, v18
	v_and_b32_e32 v19, 0xfffffc00, v19
	v_add_u32_e32 v152, v20, v16
	v_add_u32_e32 v135, v20, v17
	v_add_u32_e32 v153, v21, v18
	v_add_u32_e32 v137, v21, v19
	v_mov_b32_e32 v1, v152
	s_mov_b32 m0, s29
	s_cmp_eq_u32 s18, 1
	global_load_lds_dwordx4 v1, s[2:3]
	v_mov_b32_e32 v1, v153
	s_mov_b32 m0, s41
	s_cselect_b64 s[14:15], -1, 0
	global_load_lds_dwordx4 v1, s[2:3]
	v_mov_b32_e32 v1, v135
	s_mov_b32 m0, s45
	s_cmp_lg_u32 s18, 1
	global_load_lds_dwordx4 v1, s[2:3]
	v_mov_b32_e32 v1, v137
	s_mov_b32 m0, s48
	s_nop 0
	global_load_lds_dwordx4 v1, s[2:3]
	s_cbranch_scc1 .LBB0_1593
	s_barrier

;     __device__ __forceinline__ size_t abase(const Unit& u) const { return (size_t)((hot & 1) ? 0 : u.pm) * BM * K * 2; }
;     __device__ __forceinline__ const char* bbase(const Unit& u) const { return (const char*)Bt + (size_t)((hot & 2) ? 0 : u.pn) * BM * K * 2; }
;     __device__ __forceinline__ const char* bbase(const Unit& u) const { return (const char*)Bt + ((size_t)u.e * bstride + (size_t)u.pn * BM * K) * 2; }
; #define PG8_AOFFS(u, o0, o1) do { const int _t = otid(wv); _Pragma("unroll") for (int _i = 0; _i < 2; ++_i) { int _R, _C; stage_rc(_t * 16 + _i * 8192, _R, _C); \
;         o0[_i] = S.arow(u, _R) + (unsigned)_C * 2u; o1[_i] = S.arow(u, HALF + _R) + (unsigned)_C * 2u; } } while (0)
;     ...
;         const bool has_next = S.next(ui + 1, nxt);
;         const char* nB = has_next ? S.bbase(nxt) : cB;
;         const char* nA0 = DN ? (has_next ? Ab + S.abase(nxt) : cA0) : Ab;
;         if constexpr (!DN) {
;             if (has_next) {
;                 PG8_AOFFS(nxt, oN0, oN1);
;             } else {
; #pragma unroll
;                 for (int i = 0; i < 2; ++i) { oN0[i] = oA0[i]; oN1[i] = oA1[i]; }
;             }
.LBB0_1599:
	v_cndmask_b32_e64 v0, 0, 1, s[30:31]
	v_cmp_ne_u32_e64 s[4:5], 1, v0
	s_andn2_b64 vcc, exec, s[30:31]
	v_mov_b32_e32 v148, v152
	v_mov_b32_e32 v151, v153
	v_mov_b32_e32 v149, v135
	v_mov_b32_e32 v154, v137
	s_cbranch_vccnz .LBB0_1601
	v_mbcnt_lo_u32_b32 v0, -1, 0
	v_mbcnt_hi_u32_b32 v0, -1, v0
	v_mov_b32_e32 v6, 1
	v_add_u32_e32 v0, s93, v0
	s_add_i32 s7, s61, -1
	v_ashrrev_i32_e32 v1, 31, v0
	v_lshrrev_b32_e32 v1, 26, v1
	v_lshlrev_b32_e32 v2, 4, v0
	v_add_u32_e32 v1, v0, v1
	v_bfe_i32 v0, v0, 27, 1
	v_lshrrev_b32_e32 v0, 22, v0
	v_add_u32_e32 v0, v2, v0
	v_and_b32_e32 v0, 0xfffffc00, v0
	v_sub_u32_e32 v0, v2, v0
	v_lshrrev_b32_e32 v3, 4, v0
	v_bitop3_b32 v3, v3, v0, 32 bitop3:0x6c
	v_ashrrev_i32_e32 v0, 31, v0
	v_ashrrev_i32_e32 v1, 6, v1
	v_lshrrev_b32_e32 v0, 26, v0
	v_lshlrev_b32_e32 v4, 3, v1
	v_add_u32_e32 v0, v3, v0
	v_and_b32_e32 v4, -16, v4
	v_ashrrev_i32_e32 v0, 6, v0
	v_add_u32_e32 v4, v0, v4
	v_mul_i32_i24_e32 v0, 64, v0
	v_sub_u32_e32 v0, v3, v0
	s_lshl_b32 s23, s24, 14
	s_lshl_b32 s25, s60, 8
	v_ashrrev_i16_sdwa v0, v6, sext(v0) dst_sel:DWORD dst_unused:UNUSED_PAD src0_sel:DWORD src1_sel:BYTE_0
	s_add_i32 s25, s25, s23
	v_bfe_i32 v3, v0, 0, 16
	v_min_i32_e32 v0, s7, v4
	v_lshlrev_b32_e32 v1, 5, v1
	v_add_u32_e32 v0, s25, v0
	v_and_b32_e32 v5, 32, v1
	v_ashrrev_i32_e32 v1, 31, v0
	v_lshl_add_u64 v[0:1], v[0:1], 2, s[12:13]
	global_load_dword v148, v[0:1], off
	v_add_u32_e32 v0, 0x80, v4
	v_min_i32_e32 v0, s7, v0
	v_add_u32_e32 v0, s25, v0
	v_ashrrev_i32_e32 v1, 31, v0
	v_lshl_add_u64 v[0:1], v[0:1], 2, s[12:13]
	global_load_dword v149, v[0:1], off
	v_add_u32_e32 v0, 0x2000, v2
	v_ashrrev_i32_e32 v1, 31, v0
	v_lshrrev_b32_e32 v1, 22, v1
	v_add_u32_e32 v1, v0, v1
	v_ashrrev_i32_e32 v1, 10, v1
	v_mul_i32_i24_e32 v2, 0x400, v1
	v_sub_u32_e32 v0, v0, v2
	v_lshrrev_b32_e32 v2, 4, v0
	v_bitop3_b32 v0, v2, v0, 32 bitop3:0x6c
	v_ashrrev_i32_e32 v3, 31, v0
	v_lshrrev_b32_e32 v3, 26, v3
	v_lshlrev_b32_e32 v2, 3, v1
	v_add_u32_e32 v3, v0, v3
	v_and_b32_e32 v2, -16, v2
	v_ashrrev_i32_e32 v4, 6, v3
	v_lshlrev_b32_e32 v1, 5, v1
	v_add_u32_e32 v2, v4, v2
	v_and_b32_e32 v4, 32, v1
	v_and_b32_e32 v1, 0xc0, v3
	v_sub_u32_e32 v0, v0, v1
	v_ashrrev_i16_sdwa v0, v6, sext(v0) dst_sel:DWORD dst_unused:UNUSED_PAD src0_sel:DWORD src1_sel:BYTE_0
	v_bfe_i32 v3, v0, 0, 16
	v_min_i32_e32 v0, s7, v2
	v_add_u32_e32 v0, s25, v0
	v_ashrrev_i32_e32 v1, 31, v0
	v_lshl_add_u64 v[0:1], v[0:1], 2, s[12:13]
	global_load_dword v151, v[0:1], off
	v_add_u32_e32 v0, 0x80, v2
	v_min_i32_e32 v0, s7, v0
	v_add_u32_e32 v0, s25, v0
	v_ashrrev_i32_e32 v1, 31, v0
	v_lshl_add_u64 v[0:1], v[0:1], 2, s[12:13]
	global_load_dword v154, v[0:1], off
.LBB0_1601:
	s_ashr_i32 s25, s24, 31
	s_ashr_i32 s23, s22, 31
	s_lshl_b64 s[26:27], s[24:25], 20
	s_lshl_b64 s[34:35], s[22:23], 18
	s_add_u32 s7, s37, s34
	s_addc_u32 s23, s38, s35
	s_add_u32 s26, s7, s26
	s_addc_u32 s27, s23, s27
	s_and_b64 s[30:31], s[30:31], exec
	s_cselect_b32 s7, s27, s1
	s_cselect_b32 s23, s26, s0
	s_add_u32 s25, s0, 0x100
	v_mov_b32_e32 v32, 0
	s_addc_u32 s62, s1, 0
	s_mov_b32 s63, -2
	s_mov_b64 s[0:1], s[18:19]
	v_mov_b32_e32 v33, v32
	v_mov_b32_e32 v34, v32
	v_mov_b32_e32 v35, v32
	v_mov_b32_e32 v40, v32
	v_mov_b32_e32 v41, v32
	v_mov_b32_e32 v42, v32
	v_mov_b32_e32 v43, v32
	v_mov_b32_e32 v48, v32
	v_mov_b32_e32 v49, v32
	v_mov_b32_e32 v50, v32
	v_mov_b32_e32 v51, v32
	v_mov_b32_e32 v56, v32
	v_mov_b32_e32 v57, v32
	v_mov_b32_e32 v58, v32
	v_mov_b32_e32 v59, v32
	v_mov_b32_e32 v230, v32
	v_mov_b32_e32 v231, v32
	v_mov_b32_e32 v232, v32
	v_mov_b32_e32 v233, v32
	v_mov_b32_e32 v8, v32
	v_mov_b32_e32 v9, v32
	v_mov_b32_e32 v10, v32
	v_mov_b32_e32 v11, v32
	v_mov_b32_e32 v16, v32
	v_mov_b32_e32 v17, v32
	v_mov_b32_e32 v18, v32
	v_mov_b32_e32 v19, v32
	v_mov_b32_e32 v24, v32
	v_mov_b32_e32 v25, v32
	v_mov_b32_e32 v26, v32
	v_mov_b32_e32 v27, v32
	v_mov_b32_e32 v36, v32
	v_mov_b32_e32 v37, v32
	v_mov_b32_e32 v38, v32
	v_mov_b32_e32 v39, v32
	v_mov_b32_e32 v44, v32
	v_mov_b32_e32 v45, v32
	v_mov_b32_e32 v46, v32
	v_mov_b32_e32 v47, v32
	v_mov_b32_e32 v52, v32
	v_mov_b32_e32 v53, v32
	v_mov_b32_e32 v54, v32
	v_mov_b32_e32 v55, v32
	v_mov_b32_e32 v60, v32
	v_mov_b32_e32 v61, v32
	v_mov_b32_e32 v62, v32
	v_mov_b32_e32 v63, v32
	v_mov_b32_e32 v12, v32
	v_mov_b32_e32 v13, v32
	v_mov_b32_e32 v14, v32
	v_mov_b32_e32 v15, v32
	v_mov_b32_e32 v74, v32
	v_mov_b32_e32 v75, v32
	v_mov_b32_e32 v76, v32
	v_mov_b32_e32 v77, v32
	v_mov_b32_e32 v82, v32
	v_mov_b32_e32 v83, v32
	v_mov_b32_e32 v84, v32
	v_mov_b32_e32 v85, v32
	v_mov_b32_e32 v90, v32
	v_mov_b32_e32 v91, v32
	v_mov_b32_e32 v92, v32
	v_mov_b32_e32 v93, v32
	v_mov_b32_e32 v98, v32
	v_mov_b32_e32 v99, v32
	v_mov_b32_e32 v100, v32
	v_mov_b32_e32 v101, v32
	v_mov_b32_e32 v106, v32
	v_mov_b32_e32 v107, v32
	v_mov_b32_e32 v108, v32
	v_mov_b32_e32 v109, v32
	v_mov_b32_e32 v114, v32
	v_mov_b32_e32 v115, v32
	v_mov_b32_e32 v116, v32
	v_mov_b32_e32 v117, v32
	v_mov_b32_e32 v122, v32
	v_mov_b32_e32 v123, v32
	v_mov_b32_e32 v124, v32
	v_mov_b32_e32 v125, v32
	v_mov_b32_e32 v70, v32
	v_mov_b32_e32 v71, v32
	v_mov_b32_e32 v72, v32
	v_mov_b32_e32 v73, v32
	v_mov_b32_e32 v78, v32
	v_mov_b32_e32 v79, v32
	v_mov_b32_e32 v80, v32
	v_mov_b32_e32 v81, v32
	v_mov_b32_e32 v86, v32
	v_mov_b32_e32 v87, v32
	v_mov_b32_e32 v88, v32
	v_mov_b32_e32 v89, v32
	v_mov_b32_e32 v94, v32
	v_mov_b32_e32 v95, v32
	v_mov_b32_e32 v96, v32
	v_mov_b32_e32 v97, v32
	v_mov_b32_e32 v102, v32
	v_mov_b32_e32 v103, v32
	v_mov_b32_e32 v104, v32
	v_mov_b32_e32 v105, v32
	v_mov_b32_e32 v110, v32
	v_mov_b32_e32 v111, v32
	v_mov_b32_e32 v112, v32
	v_mov_b32_e32 v113, v32
	v_mov_b32_e32 v118, v32
	v_mov_b32_e32 v119, v32
	v_mov_b32_e32 v120, v32
	v_mov_b32_e32 v121, v32
	v_mov_b32_e32 v126, v32
	v_mov_b32_e32 v127, v32
	v_mov_b32_e32 v128, v32
	v_mov_b32_e32 v129, v32
	v_mov_b32_e32 v28, v32
	v_mov_b32_e32 v29, v32
	v_mov_b32_e32 v30, v32
	v_mov_b32_e32 v31, v32
	v_mov_b32_e32 v20, v32
	v_mov_b32_e32 v21, v32
	v_mov_b32_e32 v22, v32
	v_mov_b32_e32 v23, v32
	v_mov_b32_e32 v0, v32
	v_mov_b32_e32 v1, v32
	v_mov_b32_e32 v2, v32
	v_mov_b32_e32 v3, v32
	v_mov_b32_e32 v4, v32
	v_mov_b32_e32 v5, v32
	v_mov_b32_e32 v6, v32
	v_mov_b32_e32 v7, v32
	s_cmp_eq_u64 s[30:31], 0
	s_cbranch_scc1 .Lm1cv_skip
	s_movk_i32 s100, 0x3ff
	s_waitcnt vmcnt(0)
	v_lshlrev_b32_e32 v148, 9, v148
	v_lshlrev_b32_e32 v149, 9, v149
	v_lshlrev_b32_e32 v151, 9, v151
	v_lshlrev_b32_e32 v154, 9, v154
	v_bfi_b32 v148, s100, v152, v148
	v_bfi_b32 v149, s100, v135, v149
	v_bfi_b32 v151, s100, v153, v151
	v_bfi_b32 v154, s100, v137, v154
;     __device__ __forceinline__ void a_ready(const Unit& u, int wv) const { if (wready) wait_counter(wready + 64 * u.pm, wneed, wtmo, wv); }
; #define PG8_STAGEB(bufoff, gbase) do { unsigned _o = voffB; if constexpr (FP8) asm volatile("" : "+v"(_o)); _Pragma("unroll") for (int _i = 0; _i < 2; ++_i) \
;         __builtin_amdgcn_global_load_lds((const unsigned*)((const char*)(gbase) + _i * bstep + _o), (LAS unsigned*)(lds + (bufoff) + ldsw + _i * 8192), 16, 0, 0); } while (0)
; #define PG8_STAGE(bufoff, gbase, voff) do { _Pragma("unroll") for (int _i = 0; _i < 2; ++_i) { unsigned _o = (voff)[_i]; if constexpr (FP8) asm volatile("" : "+v"(_o));     \
;         __builtin_amdgcn_global_load_lds((const unsigned*)((const char*)(gbase) + _o), (LAS unsigned*)(lds + (bufoff) + ldsw + _i * 8192), 16, 0, 0); } } while (0)
; #define PG8_LDA(dst, b, h) do { _Pragma("unroll") for (int m = 0; m < 4; ++m) _Pragma("unroll") for (int k = 0; k < 2; ++k) dst[m][k] = *(const LAS bf16x8*)(lds + PG8_SA(b, h) + aoff + m * 2048 + k * 1024); } while (0)
; #define PG8_LDB(dst, b, h) do { _Pragma("unroll") for (int n = 0; n < 2; ++n) _Pragma("unroll") for (int k = 0; k < 2; ++k) dst[n][k] = *(const LAS bf16x8*)(lds + PG8_SB(b, h) + boff + n * 2048 + k * 1024); } while (0)
;     ...
;         for (int t = 0; t < nt; t += 2) {
;             const bool last = (t == nt - 2);
;             const char* a1 = cA0 + (size_t)(t + 1) * kstep;
;             const char* a2 = last ? nA0 : cA0 + (size_t)(t + 2) * kstep; const char* b2 = last ? nB : cB + (size_t)(t + 2) * kstep;
;             const char* a3 = a2 + kstep; const char* b3 = b2 + kstep;
;             unsigned p0[2], p1[2];
; #pragma unroll
;             for (int i = 0; i < 2; ++i) { p0[i] = DN ? voffA[i] : (last ? oN0[i] : oA0[i]); p1[i] = DN ? voffA[i] : (last ? oN1[i] : oA1[i]); }
;             if (last && has_next) S.a_ready(nxt, wv);
;     ...
;             PG8_LDB(B0, 0, 0); PG8_LDB(B1, 0, 1); PG8_SCHED; PG8_LDA(At, 0, 0); PG8_STAGE(PG8_SA(1, 1), a1 + ah, PG8_O1);
;             PG8_WAIT_V(8); PG8_WAIT_L(0); PG8_BAR; PG8_MMA(0, 0, At, B0); PG8_MMA(0, 1, At, B1); PG8_BAR; PG8_SCHED;
;             PG8_LDA(At, 0, 1); PG8_STAGEB(PG8_SB(0, 0), b2); PG8_STAGEB(PG8_SB(0, 1), b2 + hstep); PG8_STAGE(PG8_SA(0, 0), a2, p0);
;             PG8_WAIT_V(8); PG8_WAIT_L(0); PG8_BAR; PG8_MMA(1, 0, At, B0); PG8_MMA(1, 1, At, B1); PG8_BAR; PG8_SCHED;
.Lm1cv_skip:
.LBB0_1602:
	v_add_u32_e32 v64, s46, v221
	ds_read_b128 v[138:141], v64
	ds_read_b128 v[142:145], v64 offset:1024
	ds_read_b128 v[156:159], v64 offset:2048
	ds_read_b128 v[160:163], v64 offset:3072
	v_add_u32_e32 v64, s47, v221
	ds_read_b128 v[164:167], v64
	ds_read_b128 v[168:171], v64 offset:1024
	ds_read_b128 v[172:175], v64 offset:2048
	ds_read_b128 v[176:179], v64 offset:3072
	s_add_u32 s34, s0, 0x80
	s_addc_u32 s35, s1, 0
	s_cmp_eq_u32 s63, 4
	s_cselect_b64 vcc, -1, 0
	s_and_b64 s[30:31], vcc, exec
	v_cndmask_b32_e32 v130, v152, v148, vcc
	s_cselect_b32 s31, s3, s35
	s_cselect_b32 s30, s2, s34
	v_cndmask_b32_e32 v131, v135, v149, vcc
	v_cndmask_b32_e32 v132, v153, v151, vcc
	v_cndmask_b32_e32 v133, v137, v154, vcc
	s_cselect_b32 s35, s7, s62
	s_cselect_b32 s34, s23, s25
	v_mov_b32_e32 v64, v135
	ds_read_b128 v[188:191], v150
	ds_read_b128 v[192:195], v150 offset:1024
	ds_read_b128 v[196:199], v150 offset:2048
	ds_read_b128 v[200:203], v150 offset:3072
	ds_read_b128 v[204:207], v150 offset:4096
	ds_read_b128 v[208:211], v150 offset:5120
	ds_read_b128 v[222:225], v150 offset:6144
	ds_read_b128 v[226:229], v150 offset:7168
	s_add_i32 m0, s29, 0xc000
	s_nop 0
	global_load_lds_dwordx4 v64, s[0:1]
	v_mov_b32_e32 v64, v137
	s_add_i32 m0, s29, 0xe000
	s_nop 0
	global_load_lds_dwordx4 v64, s[0:1]
	s_waitcnt vmcnt(8)
	s_waitcnt lgkmcnt(0)
	s_barrier
	s_setprio 1
	s_waitcnt lgkmcnt(0)
	v_mfma_f32_16x16x128_f8f6f4 v[126:129], v[138:145], v[188:195], v[126:129]
	v_mfma_f32_16x16x128_f8f6f4 v[118:121], v[156:163], v[188:195], v[118:121]
	v_mfma_f32_16x16x128_f8f6f4 v[110:113], v[138:145], v[196:203], v[110:113]
	v_mfma_f32_16x16x128_f8f6f4 v[102:105], v[156:163], v[196:203], v[102:105]
	v_mfma_f32_16x16x128_f8f6f4 v[180:183], v[138:145], v[204:211], v[94:97]
	v_mfma_f32_16x16x128_f8f6f4 v[184:187], v[156:163], v[204:211], v[86:89]
	v_mfma_f32_16x16x128_f8f6f4 v[212:215], v[138:145], v[222:229], v[78:81]
	v_mfma_f32_16x16x128_f8f6f4 v[216:219], v[156:163], v[222:229], v[70:73]
	s_setprio 0
	s_setprio 1
	v_mfma_f32_16x16x128_f8f6f4 v[122:125], v[164:171], v[188:195], v[122:125]
	v_mfma_f32_16x16x128_f8f6f4 v[114:117], v[172:179], v[188:195], v[114:117]
	v_mfma_f32_16x16x128_f8f6f4 v[106:109], v[164:171], v[196:203], v[106:109]
	v_mfma_f32_16x16x128_f8f6f4 v[98:101], v[172:179], v[196:203], v[98:101]
	v_mfma_f32_16x16x128_f8f6f4 v[188:191], v[164:171], v[204:211], v[90:93]
	v_mfma_f32_16x16x128_f8f6f4 v[192:195], v[172:179], v[204:211], v[82:85]
	v_mfma_f32_16x16x128_f8f6f4 v[196:199], v[164:171], v[222:229], v[74:77]
	v_mfma_f32_16x16x128_f8f6f4 v[200:203], v[172:179], v[222:229], v[12:15]
	s_setprio 0
	s_barrier
	v_mov_b32_e32 v64, v220
	s_add_i32 s64, s46, s39
	ds_read_b128 v[66:69], v150 offset:16384
	ds_read_b128 v[70:73], v150 offset:17408
	ds_read_b128 v[74:77], v150 offset:18432
	ds_read_b128 v[78:81], v150 offset:19456
	ds_read_b128 v[82:85], v150 offset:20480
	ds_read_b128 v[86:89], v150 offset:21504
	ds_read_b128 v[90:93], v150 offset:22528
	ds_read_b128 v[94:97], v150 offset:23552
	s_mov_b32 m0, s64
	v_lshl_add_u64 v[146:147], s[34:35], 0, v[64:65]
	global_load_lds_dwordx4 v64, s[34:35]
	v_lshl_add_u64 v[146:147], v[146:147], 0, s[82:83]
	s_add_i32 m0, s64, 0x2000
	v_mov_b32_e32 v64, v220
	global_load_lds_dwordx4 v[146:147], off
	s_add_i32 s64, s47, s39
	v_lshl_add_u64 v[146:147], s[34:35], 0, v[64:65]
	v_mov_b32_e32 v136, v151
	v_mov_b32_e32 v151, v148
	v_mov_b32_e32 v134, v149
	v_lshl_add_u64 v[148:149], v[146:147], 0, s[66:67]
	s_mov_b32 m0, s64
	v_lshl_add_u64 v[146:147], v[146:147], 0, s[84:85]
	global_load_lds_dwordx4 v[148:149], off
	s_add_i32 m0, s64, 0x2000
	v_mov_b32_e32 v64, v130
	global_load_lds_dwordx4 v[146:147], off
	s_mov_b32 m0, s29
	s_nop 0
	global_load_lds_dwordx4 v64, s[30:31]
	v_mov_b32_e32 v64, v132
	s_mov_b32 m0, s41
	s_nop 0
	global_load_lds_dwordx4 v64, s[30:31]
	s_waitcnt vmcnt(8)
	s_waitcnt lgkmcnt(0)
	s_barrier
	s_setprio 1
	s_waitcnt lgkmcnt(0)
	v_mfma_f32_16x16x128_f8f6f4 v[60:63], v[138:145], v[66:73], v[60:63]
	v_mfma_f32_16x16x128_f8f6f4 v[52:55], v[156:163], v[66:73], v[52:55]
	v_mfma_f32_16x16x128_f8f6f4 v[24:27], v[138:145], v[82:89], v[24:27]
	v_mfma_f32_16x16x128_f8f6f4 v[230:233], v[156:163], v[90:97], v[230:233]
	v_mfma_f32_16x16x128_f8f6f4 v[204:207], v[138:145], v[74:81], v[44:47]
	v_mfma_f32_16x16x128_f8f6f4 v[208:211], v[156:163], v[74:81], v[36:39]
	v_mfma_f32_16x16x128_f8f6f4 v[222:225], v[156:163], v[82:89], v[16:19]
	v_mfma_f32_16x16x128_f8f6f4 v[226:229], v[138:145], v[90:97], v[8:11]
	s_setprio 0
	s_setprio 1
	v_mfma_f32_16x16x128_f8f6f4 v[56:59], v[164:171], v[66:73], v[56:59]
	v_mfma_f32_16x16x128_f8f6f4 v[146:149], v[172:179], v[90:97], v[4:7]
	v_mfma_f32_16x16x128_f8f6f4 v[234:237], v[172:179], v[66:73], v[48:51]
	v_mfma_f32_16x16x128_f8f6f4 v[238:241], v[164:171], v[74:81], v[40:43]
	v_mfma_f32_16x16x128_f8f6f4 v[242:245], v[172:179], v[74:81], v[32:35]
	v_mfma_f32_16x16x128_f8f6f4 v[246:249], v[164:171], v[82:89], v[28:31]
	v_mfma_f32_16x16x128_f8f6f4 v[250:253], v[172:179], v[82:89], v[20:23]
	v_mfma_f32_16x16x128_f8f6f4 v[66:69], v[164:171], v[90:97], v[0:3]
	s_setprio 0
	s_barrier
; #define PG8_STAGEB(bufoff, gbase) do { unsigned _o = voffB; if constexpr (FP8) asm volatile("" : "+v"(_o)); _Pragma("unroll") for (int _i = 0; _i < 2; ++_i) \
;         __builtin_amdgcn_global_load_lds((const unsigned*)((const char*)(gbase) + _i * bstep + _o), (LAS unsigned*)(lds + (bufoff) + ldsw + _i * 8192), 16, 0, 0); } while (0)
; #define PG8_STAGE(bufoff, gbase, voff) do { _Pragma("unroll") for (int _i = 0; _i < 2; ++_i) { unsigned _o = (voff)[_i]; if constexpr (FP8) asm volatile("" : "+v"(_o));     \
;         __builtin_amdgcn_global_load_lds((const unsigned*)((const char*)(gbase) + _o), (LAS unsigned*)(lds + (bufoff) + ldsw + _i * 8192), 16, 0, 0); } } while (0)
; #define PG8_LDA(dst, b, h) do { _Pragma("unroll") for (int m = 0; m < 4; ++m) _Pragma("unroll") for (int k = 0; k < 2; ++k) dst[m][k] = *(const LAS bf16x8*)(lds + PG8_SA(b, h) + aoff + m * 2048 + k * 1024); } while (0)
; #define PG8_LDB(dst, b, h) do { _Pragma("unroll") for (int n = 0; n < 2; ++n) _Pragma("unroll") for (int k = 0; k < 2; ++k) dst[n][k] = *(const LAS bf16x8*)(lds + PG8_SB(b, h) + boff + n * 2048 + k * 1024); } while (0)
; #define PG8_WAIT_V(n) asm volatile("s_waitcnt vmcnt(" #n ")" ::: "memory")
; #define PG8_WAIT_L(n) asm volatile("s_waitcnt lgkmcnt(" #n ")" ::: "memory")
; #define PG8_BAR __builtin_amdgcn_s_barrier()
; #define PG8_SCHED __builtin_amdgcn_sched_barrier(0)
;     ...
;             PG8_LDB(B0, 1, 0); PG8_LDB(B1, 1, 1); PG8_SCHED; PG8_LDA(At, 1, 0); PG8_STAGE(PG8_SA(0, 1), a2 + ah, p1);
;             PG8_WAIT_V(8); PG8_WAIT_L(0); PG8_BAR; PG8_MMA(0, 0, At, B0); PG8_MMA(0, 1, At, B1); PG8_BAR; PG8_SCHED;
;             PG8_LDA(At, 1, 1); PG8_STAGEB(PG8_SB(1, 0), b3); PG8_STAGEB(PG8_SB(1, 1), b3 + hstep); PG8_STAGE(PG8_SA(1, 0), a3, p0);
;             PG8_WAIT_V(8); PG8_WAIT_L(0); PG8_BAR; PG8_MMA(1, 0, At, B0); PG8_MMA(1, 1, At, B1); PG8_BAR; PG8_SCHED;
	v_add_u32_e32 v8, s52, v221
	s_nop 3
	ds_read_b128 v[0:3], v8
	ds_read_b128 v[4:7], v8 offset:1024
	ds_read_b128 v[28:31], v8 offset:2048
	ds_read_b128 v[32:35], v8 offset:3072
	v_add_u32_e32 v8, s53, v221
	ds_read_b128 v[138:141], v8
	ds_read_b128 v[142:145], v8 offset:1024
	ds_read_b128 v[156:159], v8 offset:2048
	ds_read_b128 v[160:163], v8 offset:3072
	s_mov_b32 m0, s45
	ds_read_b128 v[8:11], v150 offset:32768
	ds_read_b128 v[12:15], v150 offset:33792
	ds_read_b128 v[16:19], v150 offset:34816
	ds_read_b128 v[20:23], v150 offset:35840
	ds_read_b128 v[36:39], v150 offset:36864
	ds_read_b128 v[40:43], v150 offset:37888
	ds_read_b128 v[44:47], v150 offset:38912
	ds_read_b128 v[48:51], v150 offset:39936
	s_nop 0
	global_load_lds_dwordx4 v131, s[30:31]
	s_mov_b32 m0, s48
	s_nop 0
	global_load_lds_dwordx4 v133, s[30:31]
	s_waitcnt vmcnt(8)
	s_waitcnt lgkmcnt(0)
	s_barrier
	s_setprio 1
	s_waitcnt lgkmcnt(0)
	v_mfma_f32_16x16x128_f8f6f4 v[126:129], v[0:7], v[8:15], v[126:129]
	v_mfma_f32_16x16x128_f8f6f4 v[118:121], v[28:35], v[8:15], v[118:121]
	v_mfma_f32_16x16x128_f8f6f4 v[110:113], v[0:7], v[16:23], v[110:113]
	v_mfma_f32_16x16x128_f8f6f4 v[102:105], v[28:35], v[16:23], v[102:105]
	v_mfma_f32_16x16x128_f8f6f4 v[94:97], v[0:7], v[36:43], v[180:183]
	v_mfma_f32_16x16x128_f8f6f4 v[86:89], v[28:35], v[36:43], v[184:187]
	v_mfma_f32_16x16x128_f8f6f4 v[78:81], v[0:7], v[44:51], v[212:215]
	v_mfma_f32_16x16x128_f8f6f4 v[70:73], v[28:35], v[44:51], v[216:219]
	s_setprio 0
	s_setprio 1
	v_mfma_f32_16x16x128_f8f6f4 v[122:125], v[138:145], v[8:15], v[122:125]
	v_mfma_f32_16x16x128_f8f6f4 v[114:117], v[156:163], v[8:15], v[114:117]
	v_mfma_f32_16x16x128_f8f6f4 v[106:109], v[138:145], v[16:23], v[106:109]
	v_mfma_f32_16x16x128_f8f6f4 v[98:101], v[156:163], v[16:23], v[98:101]
	v_mfma_f32_16x16x128_f8f6f4 v[90:93], v[138:145], v[36:43], v[188:191]
	v_mfma_f32_16x16x128_f8f6f4 v[82:85], v[156:163], v[36:43], v[192:195]
	v_mfma_f32_16x16x128_f8f6f4 v[74:77], v[138:145], v[44:51], v[196:199]
	v_mfma_f32_16x16x128_f8f6f4 v[12:15], v[156:163], v[44:51], v[200:203]
	s_setprio 0
	s_barrier
	v_mov_b32_e32 v64, v220
	ds_read_b128 v[164:167], v150 offset:49152
	ds_read_b128 v[168:171], v150 offset:50176
	ds_read_b128 v[172:175], v150 offset:51200
	ds_read_b128 v[176:179], v150 offset:52224
	ds_read_b128 v[188:191], v150 offset:53248
	ds_read_b128 v[192:195], v150 offset:54272
	ds_read_b128 v[196:199], v150 offset:55296
	ds_read_b128 v[200:203], v150 offset:56320
	s_add_i32 s64, s52, s39
	v_lshl_add_u64 v[8:9], s[34:35], 0, v[64:65]
	v_lshl_add_u64 v[10:11], v[8:9], 0, s[72:73]
	s_mov_b32 m0, s64
	v_lshl_add_u64 v[8:9], v[8:9], 0, s[86:87]
	global_load_lds_dwordx4 v[10:11], off
	s_add_i32 m0, s64, 0x2000
	v_mov_b32_e32 v64, v220
	global_load_lds_dwordx4 v[8:9], off
	v_mov_b32_e32 v131, v65
	v_lshl_add_u64 v[8:9], s[34:35], 0, v[64:65]
	s_add_i32 s34, s53, s39
	v_lshl_add_u64 v[10:11], v[8:9], 0, s[74:75]
	s_mov_b32 m0, s34
	v_lshl_add_u64 v[8:9], v[8:9], 0, s[88:89]
	global_load_lds_dwordx4 v[10:11], off
	s_add_i32 m0, s34, 0x2000
	v_mov_b32_e32 v133, v65
	global_load_lds_dwordx4 v[8:9], off
	s_mov_b32 m0, s54
	v_lshl_add_u64 v[8:9], s[30:31], 0, v[130:131]
	v_lshl_add_u64 v[8:9], v[8:9], 0, s[72:73]
	global_load_lds_dwordx4 v[8:9], off
	s_mov_b32 m0, s55
	v_lshl_add_u64 v[8:9], s[30:31], 0, v[132:133]
	v_lshl_add_u64 v[8:9], v[8:9], 0, s[72:73]
	global_load_lds_dwordx4 v[8:9], off
	s_waitcnt vmcnt(8)
	s_waitcnt lgkmcnt(0)
	s_barrier
	s_setprio 1
	s_waitcnt lgkmcnt(0)
	v_mfma_f32_16x16x128_f8f6f4 v[60:63], v[0:7], v[164:171], v[60:63]
	v_mfma_f32_16x16x128_f8f6f4 v[52:55], v[28:35], v[164:171], v[52:55]
	v_mfma_f32_16x16x128_f8f6f4 v[44:47], v[0:7], v[172:179], v[204:207]
	v_mfma_f32_16x16x128_f8f6f4 v[36:39], v[28:35], v[172:179], v[208:211]
	v_mfma_f32_16x16x128_f8f6f4 v[24:27], v[0:7], v[188:195], v[24:27]
	v_mfma_f32_16x16x128_f8f6f4 v[16:19], v[28:35], v[188:195], v[222:225]
	v_mfma_f32_16x16x128_f8f6f4 v[8:11], v[0:7], v[196:203], v[226:229]
	v_mfma_f32_16x16x128_f8f6f4 v[230:233], v[28:35], v[196:203], v[230:233]
	s_setprio 0
	s_setprio 1
	v_mfma_f32_16x16x128_f8f6f4 v[56:59], v[138:145], v[164:171], v[56:59]
	v_mfma_f32_16x16x128_f8f6f4 v[48:51], v[156:163], v[164:171], v[234:237]
	v_mfma_f32_16x16x128_f8f6f4 v[40:43], v[138:145], v[172:179], v[238:241]
	v_mfma_f32_16x16x128_f8f6f4 v[32:35], v[156:163], v[172:179], v[242:245]
	v_mfma_f32_16x16x128_f8f6f4 v[28:31], v[138:145], v[188:195], v[246:249]
	v_mfma_f32_16x16x128_f8f6f4 v[20:23], v[156:163], v[188:195], v[250:253]
	v_mfma_f32_16x16x128_f8f6f4 v[0:3], v[138:145], v[196:203], v[66:69]
	v_mfma_f32_16x16x128_f8f6f4 v[4:7], v[156:163], v[196:203], v[146:149]
	s_nop 6
	v_mov_b32_e32 v149, v134
	v_mov_b32_e32 v148, v151
	v_mov_b32_e32 v151, v136
	s_setprio 0
	s_barrier
	s_add_i32 s63, s63, 2
	s_add_u32 s25, s25, 0x100
	s_addc_u32 s62, s62, 0
	s_add_u32 s0, s0, 0x100
	s_addc_u32 s1, s1, 0
	s_cmp_gt_u32 s63, 5
	s_cbranch_scc0 .LBB0_1602
	s_and_b64 vcc, exec, s[20:21]
	s_cbranch_vccz .LBB0_1605
	s_barrier

;     __device__ __forceinline__ size_t abase(const Unit& u) const { return (size_t)((hot & 1) ? 0 : u.pm) * BM * K * 2; }
;     __device__ __forceinline__ unsigned arow(const Unit& u, int r) const { return (unsigned)(((hot & 1) ? 0 : u.pm * BM) + r) * (unsigned)(K * 2); }
;     __device__ __forceinline__ const char* bbase(const Unit& u) const { return (const char*)Bt + (size_t)((hot & 2) ? 0 : u.pn) * BM * K * 2; }
;     __device__ __forceinline__ const char* bbase(const Unit& u) const { return (const char*)Bt + ((size_t)u.e * bstride + (size_t)u.pn * BM * K) * 2; }
; #define PG8_AOFFS(u, o0, o1) do { const int _t = otid(wv); _Pragma("unroll") for (int _i = 0; _i < 2; ++_i) { int _R, _C; stage_rc(_t * 16 + _i * 8192, _R, _C); \
;         o0[_i] = S.arow(u, _R) + (unsigned)_C * 2u; o1[_i] = S.arow(u, HALF + _R) + (unsigned)_C * 2u; } } while (0)
;     __device__ __forceinline__ unsigned arow(const Unit& u, int r) const {
;         const int idx = r < u.rows ? r : u.rows - 1; const int slot = list[u.e * LCAP + u.pm * BM + idx];
;         return (unsigned)(TOKEN_ROWS ? (slot >> 1) : slot) * (unsigned)(K * 2);
;     ...
;         const bool has_next = S.next(ui + 1, nxt);
;         const char* nB = has_next ? S.bbase(nxt) : cB;
;         const char* nA0 = DN ? (has_next ? Ab + S.abase(nxt) : cA0) : Ab;
;         if constexpr (!DN) {
;             if (has_next) {
;                 PG8_AOFFS(nxt, oN0, oN1);
;             } else {
; #pragma unroll
;                 for (int i = 0; i < 2; ++i) { oN0[i] = oA0[i]; oN1[i] = oA1[i]; }
;             }
.LBB0_1655:
	s_movk_i32 s100, 0x3ff
	v_lshrrev_b32_e32 v230, 10, v132
	v_lshrrev_b32_e32 v231, 10, v134
	v_lshrrev_b32_e32 v232, 10, v136
	v_lshrrev_b32_e32 v233, 10, v138
	v_cndmask_b32_e64 v0, 0, 1, s[28:29]
	v_cmp_ne_u32_e64 s[4:5], 1, v0
	s_andn2_b64 vcc, exec, s[28:29]
	v_mov_b32_e32 v142, v132
	v_mov_b32_e32 v144, v136
	v_mov_b32_e32 v143, v134
	v_mov_b32_e32 v145, v138
	s_cbranch_vccnz .LBB0_1657
	v_mbcnt_lo_u32_b32 v0, -1, 0
	v_mbcnt_hi_u32_b32 v0, -1, v0
	s_add_i32 s1, s65, -1
	v_add_u32_e32 v0, s93, v0
	s_lshl_b32 s6, s22, 14
	v_ashrrev_i32_e32 v1, 31, v0
	v_lshrrev_b32_e32 v1, 26, v1
	v_lshlrev_b32_e32 v2, 4, v0
	v_add_u32_e32 v1, v0, v1
	v_bfe_i32 v0, v0, 27, 1
	v_lshrrev_b32_e32 v0, 22, v0
	v_add_u32_e32 v0, v2, v0
	v_and_b32_e32 v0, 0xfffffc00, v0
	v_sub_u32_e32 v0, v2, v0
	v_lshrrev_b32_e32 v3, 4, v0
	v_bitop3_b32 v3, v3, v0, 32 bitop3:0x6c
	v_ashrrev_i32_e32 v0, 31, v0
	v_ashrrev_i32_e32 v1, 6, v1
	v_lshrrev_b32_e32 v0, 26, v0
	v_lshlrev_b32_e32 v4, 3, v1
	v_add_u32_e32 v0, v3, v0
	v_and_b32_e32 v4, -16, v4
	v_ashrrev_i32_e32 v0, 6, v0
	v_add_u32_e32 v4, v0, v4
	v_mul_i32_i24_e32 v0, 64, v0
	v_sub_u32_e32 v0, v3, v0
	s_lshl_b32 s7, s64, 8
	v_ashrrev_i16_sdwa v0, v227, sext(v0) dst_sel:DWORD dst_unused:UNUSED_PAD src0_sel:DWORD src1_sel:BYTE_0
	s_add_i32 s7, s7, s6
	v_bfe_i32 v3, v0, 0, 16
	v_min_i32_e32 v0, s1, v4
	v_lshlrev_b32_e32 v1, 5, v1
	v_add_u32_e32 v0, s7, v0
	v_and_b32_e32 v5, 32, v1
	v_ashrrev_i32_e32 v1, 31, v0
	v_lshl_add_u64 v[0:1], v[0:1], 2, s[12:13]
	global_load_dword v230, v[0:1], off
	v_add_lshl_u32 v3, v5, v3, 1
	v_add_u32_e32 v0, 0x80, v4
	v_min_i32_e32 v0, s1, v0
	v_add_u32_e32 v0, s7, v0
	v_ashrrev_i32_e32 v1, 31, v0
	v_lshl_add_u64 v[0:1], v[0:1], 2, s[12:13]
	global_load_dword v231, v[0:1], off
	v_add_u32_e32 v0, 0x2000, v2
	v_ashrrev_i32_e32 v1, 31, v0
	v_lshrrev_b32_e32 v1, 22, v1
	v_add_u32_e32 v1, v0, v1
	v_ashrrev_i32_e32 v1, 10, v1
	v_mul_i32_i24_e32 v2, 0x400, v1
	v_sub_u32_e32 v0, v0, v2
	v_lshrrev_b32_e32 v2, 4, v0
	v_bitop3_b32 v0, v2, v0, 32 bitop3:0x6c
	v_ashrrev_i32_e32 v3, 31, v0
	v_lshrrev_b32_e32 v3, 26, v3
	v_lshlrev_b32_e32 v2, 3, v1
	v_add_u32_e32 v3, v0, v3
	v_and_b32_e32 v2, -16, v2
	v_ashrrev_i32_e32 v4, 6, v3
	v_lshlrev_b32_e32 v1, 5, v1
	v_add_u32_e32 v2, v4, v2
	v_and_b32_e32 v4, 32, v1
	v_and_b32_e32 v1, 0xc0, v3
	v_sub_u32_e32 v0, v0, v1
	v_ashrrev_i16_sdwa v0, v227, sext(v0) dst_sel:DWORD dst_unused:UNUSED_PAD src0_sel:DWORD src1_sel:BYTE_0
	v_bfe_i32 v3, v0, 0, 16
	v_min_i32_e32 v0, s1, v2
	v_add_u32_e32 v0, s7, v0
	v_ashrrev_i32_e32 v1, 31, v0
	v_lshl_add_u64 v[0:1], v[0:1], 2, s[12:13]
	global_load_dword v232, v[0:1], off
	v_add_lshl_u32 v3, v4, v3, 1
	v_add_u32_e32 v0, 0x80, v2
	v_min_i32_e32 v0, s1, v0
	v_add_u32_e32 v0, s7, v0
	v_ashrrev_i32_e32 v1, 31, v0
	v_lshl_add_u64 v[0:1], v[0:1], 2, s[12:13]
	global_load_dword v233, v[0:1], off

;     __device__ __forceinline__ void a_ready(const Unit& u, int wv) const { if (wready) wait_counter(wready + 64 * u.pm, wneed, wtmo, wv); }
; #define PG8_STAGE(bufoff, gbase, voff) do { _Pragma("unroll") for (int _i = 0; _i < 2; ++_i) { unsigned _o = (voff)[_i]; if constexpr (FP8) asm volatile("" : "+v"(_o));     \
;         __builtin_amdgcn_global_load_lds((const unsigned*)((const char*)(gbase) + _o), (LAS unsigned*)(lds + (bufoff) + ldsw + _i * 8192), 16, 0, 0); } } while (0)
; #define PG8_LDA(dst, b, h) do { _Pragma("unroll") for (int m = 0; m < 4; ++m) _Pragma("unroll") for (int k = 0; k < 2; ++k) dst[m][k] = *(const LAS bf16x8*)(lds + PG8_SA(b, h) + aoff + m * 2048 + k * 1024); } while (0)
; #define PG8_LDB(dst, b, h) do { _Pragma("unroll") for (int n = 0; n < 2; ++n) _Pragma("unroll") for (int k = 0; k < 2; ++k) dst[n][k] = *(const LAS bf16x8*)(lds + PG8_SB(b, h) + boff + n * 2048 + k * 1024); } while (0)
; #define PG8_WAIT_V(n) asm volatile("s_waitcnt vmcnt(" #n ")" ::: "memory")
; #define PG8_WAIT_L(n) asm volatile("s_waitcnt lgkmcnt(" #n ")" ::: "memory")
; #define PG8_BAR __builtin_amdgcn_s_barrier()
; #define PG8_SCHED __builtin_amdgcn_sched_barrier(0)
;     ...
;         for (int t = 0; t < nt; t += 2) {
;             const bool last = (t == nt - 2);
;             const char* a1 = cA0 + (size_t)(t + 1) * kstep;
;             const char* a2 = last ? nA0 : cA0 + (size_t)(t + 2) * kstep; const char* b2 = last ? nB : cB + (size_t)(t + 2) * kstep;
;             const char* a3 = a2 + kstep; const char* b3 = b2 + kstep;
;             unsigned p0[2], p1[2];
; #pragma unroll
;             for (int i = 0; i < 2; ++i) { p0[i] = DN ? voffA[i] : (last ? oN0[i] : oA0[i]); p1[i] = DN ? voffA[i] : (last ? oN1[i] : oA1[i]); }
;             if (last && has_next) S.a_ready(nxt, wv);
;     ...
;             PG8_LDB(B0, 0, 0); PG8_LDB(B1, 0, 1); PG8_SCHED; PG8_LDA(At, 0, 0); PG8_STAGE(PG8_SA(1, 1), a1 + ah, PG8_O1);
;             PG8_WAIT_V(8); PG8_WAIT_L(0); PG8_BAR; PG8_MMA(0, 0, At, B0); PG8_MMA(0, 1, At, B1); PG8_BAR; PG8_SCHED;
.LBB0_1661:
	s_lshl_b32 s36, s68, 7
	s_add_u32 s34, s10, s36
	s_addc_u32 s35, s11, 0
	v_add_u32_e32 v137, s46, v140
	s_add_u32 s37, s34, 0x100
	ds_read_b128 v[146:149], v137
	ds_read_b128 v[150:153], v137 offset:1024
	ds_read_b128 v[154:157], v137 offset:2048
	ds_read_b128 v[158:161], v137 offset:3072
	v_add_u32_e32 v137, s47, v140
	s_addc_u32 s40, s35, 0
	ds_read_b128 v[162:165], v137
	ds_read_b128 v[166:169], v137 offset:1024
	ds_read_b128 v[170:173], v137 offset:2048
	ds_read_b128 v[174:177], v137 offset:3072
	s_and_b64 s[30:31], s[6:7], exec
	s_cselect_b32 s31, s11, s40
	s_cselect_b32 s30, s10, s37
	s_add_u32 s36, s24, s36
	s_addc_u32 s37, s25, 0
	s_add_u32 s36, s36, 0x100
	s_addc_u32 s37, s37, 0
	v_lshlrev_b32_e32 v142, 10, v230
	v_lshlrev_b32_e32 v143, 10, v231
	v_lshlrev_b32_e32 v144, 10, v232
	v_lshlrev_b32_e32 v145, 10, v233
	v_bfi_b32 v142, s100, v132, v142
	v_bfi_b32 v143, s100, v134, v143
	v_bfi_b32 v144, s100, v136, v144
	v_bfi_b32 v145, s100, v138, v145
	v_cndmask_b32_e64 v64, v132, v142, s[6:7]
	v_cndmask_b32_e64 v133, v134, v143, s[6:7]
	v_cndmask_b32_e64 v210, v136, v144, s[6:7]
	v_cndmask_b32_e64 v137, v138, v145, s[6:7]
	s_and_b64 s[6:7], s[6:7], exec
	s_cselect_b32 s7, s1, s37
	s_cselect_b32 s6, s19, s36
	v_lshl_add_u64 v[212:213], s[34:35], 0, v[134:135]
	v_lshl_add_u64 v[212:213], v[212:213], 0, s[72:73]
	s_add_i32 m0, s48, 0xc000
	ds_read_b128 v[178:181], v141
	ds_read_b128 v[182:185], v141 offset:1024
	ds_read_b128 v[186:189], v141 offset:2048
	ds_read_b128 v[190:193], v141 offset:3072
	ds_read_b128 v[194:197], v141 offset:4096
	ds_read_b128 v[198:201], v141 offset:5120
	ds_read_b128 v[202:205], v141 offset:6144
	ds_read_b128 v[206:209], v141 offset:7168
	global_load_lds_dwordx4 v[212:213], off
	v_lshl_add_u64 v[212:213], s[34:35], 0, v[138:139]
	v_lshl_add_u64 v[212:213], v[212:213], 0, s[72:73]
	s_add_i32 m0, s48, 0xe000
	s_nop 0
	global_load_lds_dwordx4 v[212:213], off
	s_waitcnt vmcnt(8)
	s_waitcnt lgkmcnt(0)
	s_barrier
	s_setprio 1
	s_waitcnt lgkmcnt(0)
	v_mfma_f32_16x16x32_bf16 v[126:129], v[146:149], v[178:181], v[126:129]
	v_mfma_f32_16x16x32_bf16 v[122:125], v[154:157], v[178:181], v[122:125]
	v_mfma_f32_16x16x32_bf16 v[118:121], v[146:149], v[186:189], v[118:121]
	v_mfma_f32_16x16x32_bf16 v[114:117], v[154:157], v[186:189], v[114:117]
	v_mfma_f32_16x16x32_bf16 v[94:97], v[146:149], v[194:197], v[94:97]
	v_mfma_f32_16x16x32_bf16 v[90:93], v[154:157], v[194:197], v[90:93]
	v_mfma_f32_16x16x32_bf16 v[86:89], v[146:149], v[202:205], v[86:89]
	v_mfma_f32_16x16x32_bf16 v[82:85], v[154:157], v[202:205], v[82:85]
	v_mfma_f32_16x16x32_bf16 v[126:129], v[150:153], v[182:185], v[126:129]
	v_mfma_f32_16x16x32_bf16 v[122:125], v[158:161], v[182:185], v[122:125]
	v_mfma_f32_16x16x32_bf16 v[118:121], v[150:153], v[190:193], v[118:121]
	v_mfma_f32_16x16x32_bf16 v[114:117], v[158:161], v[190:193], v[114:117]
	v_mfma_f32_16x16x32_bf16 v[94:97], v[150:153], v[198:201], v[94:97]
	v_mfma_f32_16x16x32_bf16 v[90:93], v[158:161], v[198:201], v[90:93]
	v_mfma_f32_16x16x32_bf16 v[86:89], v[150:153], v[206:209], v[86:89]
	v_mfma_f32_16x16x32_bf16 v[82:85], v[158:161], v[206:209], v[82:85]
	s_setprio 0
	s_setprio 1
	v_mfma_f32_16x16x32_bf16 v[110:113], v[162:165], v[178:181], v[110:113]
	v_mfma_f32_16x16x32_bf16 v[106:109], v[170:173], v[178:181], v[106:109]
	v_mfma_f32_16x16x32_bf16 v[102:105], v[162:165], v[186:189], v[102:105]
	v_mfma_f32_16x16x32_bf16 v[98:101], v[170:173], v[186:189], v[98:101]
	v_mfma_f32_16x16x32_bf16 v[78:81], v[162:165], v[194:197], v[78:81]
	v_mfma_f32_16x16x32_bf16 v[74:77], v[170:173], v[194:197], v[74:77]
	v_mfma_f32_16x16x32_bf16 v[70:73], v[162:165], v[202:205], v[70:73]
	v_mfma_f32_16x16x32_bf16 v[66:69], v[170:173], v[202:205], v[66:69]
	v_mfma_f32_16x16x32_bf16 v[110:113], v[166:169], v[182:185], v[110:113]
	v_mfma_f32_16x16x32_bf16 v[106:109], v[174:177], v[182:185], v[106:109]
	v_mfma_f32_16x16x32_bf16 v[102:105], v[166:169], v[190:193], v[102:105]
	v_mfma_f32_16x16x32_bf16 v[98:101], v[174:177], v[190:193], v[98:101]
	v_mfma_f32_16x16x32_bf16 v[78:81], v[166:169], v[198:201], v[78:81]
	v_mfma_f32_16x16x32_bf16 v[74:77], v[174:177], v[198:201], v[74:77]
	v_mfma_f32_16x16x32_bf16 v[70:73], v[166:169], v[206:209], v[70:73]
	v_mfma_f32_16x16x32_bf16 v[66:69], v[174:177], v[206:209], v[66:69]
	s_setprio 0
	s_barrier
	v_lshl_add_u64 v[212:213], s[6:7], 0, v[130:131]
	s_add_i32 s6, s46, s21
	s_mov_b32 m0, s6
	ds_read_b128 v[178:181], v141 offset:16384
	ds_read_b128 v[182:185], v141 offset:17408
	ds_read_b128 v[186:189], v141 offset:18432
	ds_read_b128 v[190:193], v141 offset:19456
	ds_read_b128 v[194:197], v141 offset:20480
	ds_read_b128 v[198:201], v141 offset:21504
	ds_read_b128 v[202:205], v141 offset:22528
	ds_read_b128 v[206:209], v141 offset:23552
	global_load_lds_dwordx4 v[212:213], off
	v_lshl_add_u64 v[214:215], v[212:213], 0, s[82:83]
	s_add_i32 m0, s6, 0x2000
	s_add_i32 s6, s47, s21
	global_load_lds_dwordx4 v[214:215], off
	v_lshl_add_u64 v[214:215], v[212:213], 0, s[66:67]
	s_mov_b32 m0, s6
	v_mov_b32_e32 v211, v65
	global_load_lds_dwordx4 v[214:215], off
	v_lshl_add_u64 v[214:215], v[212:213], 0, s[84:85]
	s_add_i32 m0, s6, 0x2000
	s_nop 0
	global_load_lds_dwordx4 v[214:215], off
	s_mov_b32 m0, s48
	v_lshl_add_u64 v[214:215], s[30:31], 0, v[64:65]
	global_load_lds_dwordx4 v64, s[30:31]
	s_mov_b32 m0, s49
	s_nop 0
	global_load_lds_dwordx4 v210, s[30:31]
	s_waitcnt vmcnt(8)
	s_waitcnt lgkmcnt(0)
	v_lshl_add_u64 v[210:211], s[30:31], 0, v[210:211]
	s_barrier
; #define PG8_STAGEB(bufoff, gbase) do { unsigned _o = voffB; if constexpr (FP8) asm volatile("" : "+v"(_o)); _Pragma("unroll") for (int _i = 0; _i < 2; ++_i) \
;         __builtin_amdgcn_global_load_lds((const unsigned*)((const char*)(gbase) + _i * bstep + _o), (LAS unsigned*)(lds + (bufoff) + ldsw + _i * 8192), 16, 0, 0); } while (0)
; #define PG8_STAGE(bufoff, gbase, voff) do { _Pragma("unroll") for (int _i = 0; _i < 2; ++_i) { unsigned _o = (voff)[_i]; if constexpr (FP8) asm volatile("" : "+v"(_o));     \
;         __builtin_amdgcn_global_load_lds((const unsigned*)((const char*)(gbase) + _o), (LAS unsigned*)(lds + (bufoff) + ldsw + _i * 8192), 16, 0, 0); } } while (0)
; #define PG8_LDA(dst, b, h) do { _Pragma("unroll") for (int m = 0; m < 4; ++m) _Pragma("unroll") for (int k = 0; k < 2; ++k) dst[m][k] = *(const LAS bf16x8*)(lds + PG8_SA(b, h) + aoff + m * 2048 + k * 1024); } while (0)
; #define PG8_LDB(dst, b, h) do { _Pragma("unroll") for (int n = 0; n < 2; ++n) _Pragma("unroll") for (int k = 0; k < 2; ++k) dst[n][k] = *(const LAS bf16x8*)(lds + PG8_SB(b, h) + boff + n * 2048 + k * 1024); } while (0)
; #define PG8_WAIT_V(n) asm volatile("s_waitcnt vmcnt(" #n ")" ::: "memory")
; #define PG8_WAIT_L(n) asm volatile("s_waitcnt lgkmcnt(" #n ")" ::: "memory")
; #define PG8_BAR __builtin_amdgcn_s_barrier()
; #define PG8_SCHED __builtin_amdgcn_sched_barrier(0)
;     ...
;             PG8_WAIT_V(8); PG8_WAIT_L(0); PG8_BAR; PG8_MMA(0, 0, At, B0); PG8_MMA(0, 1, At, B1); PG8_BAR; PG8_SCHED;
;             PG8_LDA(At, 0, 1); PG8_STAGEB(PG8_SB(0, 0), b2); PG8_STAGEB(PG8_SB(0, 1), b2 + hstep); PG8_STAGE(PG8_SA(0, 0), a2, p0);
;             PG8_WAIT_V(8); PG8_WAIT_L(0); PG8_BAR; PG8_MMA(1, 0, At, B0); PG8_MMA(1, 1, At, B1); PG8_BAR; PG8_SCHED;
;             PG8_LDB(B0, 1, 0); PG8_LDB(B1, 1, 1); PG8_SCHED; PG8_LDA(At, 1, 0); PG8_STAGE(PG8_SA(0, 1), a2 + ah, p1);
;             PG8_WAIT_V(8); PG8_WAIT_L(0); PG8_BAR; PG8_MMA(0, 0, At, B0); PG8_MMA(0, 1, At, B1); PG8_BAR; PG8_SCHED;
	s_setprio 1
	s_waitcnt lgkmcnt(0)
	v_mfma_f32_16x16x32_bf16 v[60:63], v[146:149], v[178:181], v[60:63]
	v_mfma_f32_16x16x32_bf16 v[56:59], v[154:157], v[178:181], v[56:59]
	v_mfma_f32_16x16x32_bf16 v[52:55], v[146:149], v[186:189], v[52:55]
	v_mfma_f32_16x16x32_bf16 v[48:51], v[154:157], v[186:189], v[48:51]
	v_mfma_f32_16x16x32_bf16 v[20:23], v[146:149], v[194:197], v[20:23]
	v_mfma_f32_16x16x32_bf16 v[16:19], v[154:157], v[194:197], v[16:19]
	v_mfma_f32_16x16x32_bf16 v[4:7], v[146:149], v[202:205], v[4:7]
	v_mfma_f32_16x16x32_bf16 v[0:3], v[154:157], v[202:205], v[0:3]
	v_mfma_f32_16x16x32_bf16 v[60:63], v[150:153], v[182:185], v[60:63]
	v_mfma_f32_16x16x32_bf16 v[56:59], v[158:161], v[182:185], v[56:59]
	v_mfma_f32_16x16x32_bf16 v[52:55], v[150:153], v[190:193], v[52:55]
	v_mfma_f32_16x16x32_bf16 v[48:51], v[158:161], v[190:193], v[48:51]
	v_mfma_f32_16x16x32_bf16 v[20:23], v[150:153], v[198:201], v[20:23]
	v_mfma_f32_16x16x32_bf16 v[16:19], v[158:161], v[198:201], v[16:19]
	v_mfma_f32_16x16x32_bf16 v[4:7], v[150:153], v[206:209], v[4:7]
	v_mfma_f32_16x16x32_bf16 v[0:3], v[158:161], v[206:209], v[0:3]
	s_setprio 0
	s_setprio 1
	v_mfma_f32_16x16x32_bf16 v[44:47], v[162:165], v[178:181], v[44:47]
	v_mfma_f32_16x16x32_bf16 v[40:43], v[170:173], v[178:181], v[40:43]
	v_mfma_f32_16x16x32_bf16 v[36:39], v[162:165], v[186:189], v[36:39]
	v_mfma_f32_16x16x32_bf16 v[32:35], v[170:173], v[186:189], v[32:35]
	v_mfma_f32_16x16x32_bf16 v[24:27], v[162:165], v[194:197], v[24:27]
	v_mfma_f32_16x16x32_bf16 v[28:31], v[170:173], v[194:197], v[28:31]
	v_mfma_f32_16x16x32_bf16 v[8:11], v[162:165], v[202:205], v[8:11]
	v_mfma_f32_16x16x32_bf16 v[12:15], v[170:173], v[202:205], v[12:15]
	v_mfma_f32_16x16x32_bf16 v[44:47], v[166:169], v[182:185], v[44:47]
	v_mfma_f32_16x16x32_bf16 v[40:43], v[174:177], v[182:185], v[40:43]
	v_mfma_f32_16x16x32_bf16 v[36:39], v[166:169], v[190:193], v[36:39]
	v_mfma_f32_16x16x32_bf16 v[32:35], v[174:177], v[190:193], v[32:35]
	v_mfma_f32_16x16x32_bf16 v[24:27], v[166:169], v[198:201], v[24:27]
	v_mfma_f32_16x16x32_bf16 v[28:31], v[174:177], v[198:201], v[28:31]
	v_mfma_f32_16x16x32_bf16 v[8:11], v[166:169], v[206:209], v[8:11]
	v_mfma_f32_16x16x32_bf16 v[12:15], v[174:177], v[206:209], v[12:15]
	s_setprio 0
	s_barrier
	v_add_u32_e32 v64, s52, v140
	ds_read_b128 v[146:149], v64
	ds_read_b128 v[150:153], v64 offset:1024
	ds_read_b128 v[154:157], v64 offset:2048
	ds_read_b128 v[158:161], v64 offset:3072
	v_add_u32_e32 v64, s53, v140
	ds_read_b128 v[162:165], v64
	ds_read_b128 v[166:169], v64 offset:1024
	ds_read_b128 v[170:173], v64 offset:2048
	ds_read_b128 v[174:177], v64 offset:3072
	s_mov_b32 m0, s50
	ds_read_b128 v[178:181], v141 offset:32768
	ds_read_b128 v[182:185], v141 offset:33792
	ds_read_b128 v[186:189], v141 offset:34816
	ds_read_b128 v[190:193], v141 offset:35840
	ds_read_b128 v[194:197], v141 offset:36864
	ds_read_b128 v[198:201], v141 offset:37888
	ds_read_b128 v[202:205], v141 offset:38912
	ds_read_b128 v[206:209], v141 offset:39936
	global_load_lds_dwordx4 v133, s[30:31]
	s_mov_b32 m0, s54
	s_nop 0
	global_load_lds_dwordx4 v137, s[30:31]
	s_waitcnt vmcnt(8)
	s_waitcnt lgkmcnt(0)
	s_barrier
	s_setprio 1
	s_waitcnt lgkmcnt(0)
	v_mfma_f32_16x16x32_bf16 v[126:129], v[146:149], v[178:181], v[126:129]
	v_mfma_f32_16x16x32_bf16 v[122:125], v[154:157], v[178:181], v[122:125]
	v_mfma_f32_16x16x32_bf16 v[118:121], v[146:149], v[186:189], v[118:121]
	v_mfma_f32_16x16x32_bf16 v[114:117], v[154:157], v[186:189], v[114:117]
	v_mfma_f32_16x16x32_bf16 v[94:97], v[146:149], v[194:197], v[94:97]
	v_mfma_f32_16x16x32_bf16 v[90:93], v[154:157], v[194:197], v[90:93]
	v_mfma_f32_16x16x32_bf16 v[86:89], v[146:149], v[202:205], v[86:89]
	v_mfma_f32_16x16x32_bf16 v[82:85], v[154:157], v[202:205], v[82:85]
	v_mfma_f32_16x16x32_bf16 v[126:129], v[150:153], v[182:185], v[126:129]
	v_mfma_f32_16x16x32_bf16 v[122:125], v[158:161], v[182:185], v[122:125]
	v_mfma_f32_16x16x32_bf16 v[118:121], v[150:153], v[190:193], v[118:121]
	v_mfma_f32_16x16x32_bf16 v[114:117], v[158:161], v[190:193], v[114:117]
	v_mfma_f32_16x16x32_bf16 v[94:97], v[150:153], v[198:201], v[94:97]
	v_mfma_f32_16x16x32_bf16 v[90:93], v[158:161], v[198:201], v[90:93]
	v_mfma_f32_16x16x32_bf16 v[86:89], v[150:153], v[206:209], v[86:89]
	v_mfma_f32_16x16x32_bf16 v[82:85], v[158:161], v[206:209], v[82:85]
	s_setprio 0
	s_setprio 1
	v_mfma_f32_16x16x32_bf16 v[110:113], v[162:165], v[178:181], v[110:113]
	v_mfma_f32_16x16x32_bf16 v[106:109], v[170:173], v[178:181], v[106:109]
	v_mfma_f32_16x16x32_bf16 v[102:105], v[162:165], v[186:189], v[102:105]
	v_mfma_f32_16x16x32_bf16 v[98:101], v[170:173], v[186:189], v[98:101]
	v_mfma_f32_16x16x32_bf16 v[78:81], v[162:165], v[194:197], v[78:81]
	v_mfma_f32_16x16x32_bf16 v[74:77], v[170:173], v[194:197], v[74:77]
	v_mfma_f32_16x16x32_bf16 v[70:73], v[162:165], v[202:205], v[70:73]
	v_mfma_f32_16x16x32_bf16 v[66:69], v[170:173], v[202:205], v[66:69]
	v_mfma_f32_16x16x32_bf16 v[110:113], v[166:169], v[182:185], v[110:113]
	v_mfma_f32_16x16x32_bf16 v[106:109], v[174:177], v[182:185], v[106:109]
	v_mfma_f32_16x16x32_bf16 v[102:105], v[166:169], v[190:193], v[102:105]
	v_mfma_f32_16x16x32_bf16 v[98:101], v[174:177], v[190:193], v[98:101]
	v_mfma_f32_16x16x32_bf16 v[78:81], v[166:169], v[198:201], v[78:81]
	v_mfma_f32_16x16x32_bf16 v[74:77], v[174:177], v[198:201], v[74:77]
	v_mfma_f32_16x16x32_bf16 v[70:73], v[166:169], v[206:209], v[70:73]
	v_mfma_f32_16x16x32_bf16 v[66:69], v[174:177], v[206:209], v[66:69]
	s_setprio 0
	s_barrier
; #define PG8_STAGEB(bufoff, gbase) do { unsigned _o = voffB; if constexpr (FP8) asm volatile("" : "+v"(_o)); _Pragma("unroll") for (int _i = 0; _i < 2; ++_i) \
;         __builtin_amdgcn_global_load_lds((const unsigned*)((const char*)(gbase) + _i * bstep + _o), (LAS unsigned*)(lds + (bufoff) + ldsw + _i * 8192), 16, 0, 0); } while (0)
; #define PG8_STAGE(bufoff, gbase, voff) do { _Pragma("unroll") for (int _i = 0; _i < 2; ++_i) { unsigned _o = (voff)[_i]; if constexpr (FP8) asm volatile("" : "+v"(_o));     \
;         __builtin_amdgcn_global_load_lds((const unsigned*)((const char*)(gbase) + _o), (LAS unsigned*)(lds + (bufoff) + ldsw + _i * 8192), 16, 0, 0); } } while (0)
; #define PG8_LDA(dst, b, h) do { _Pragma("unroll") for (int m = 0; m < 4; ++m) _Pragma("unroll") for (int k = 0; k < 2; ++k) dst[m][k] = *(const LAS bf16x8*)(lds + PG8_SA(b, h) + aoff + m * 2048 + k * 1024); } while (0)
; #define PG8_WAIT_V(n) asm volatile("s_waitcnt vmcnt(" #n ")" ::: "memory")
; #define PG8_WAIT_L(n) asm volatile("s_waitcnt lgkmcnt(" #n ")" ::: "memory")
; #define PG8_BAR __builtin_amdgcn_s_barrier()
; #define PG8_SCHED __builtin_amdgcn_sched_barrier(0)
;     ...
;         for (int t = 0; t < nt; t += 2) {
;     ...
;             PG8_LDA(At, 1, 1); PG8_STAGEB(PG8_SB(1, 0), b3); PG8_STAGEB(PG8_SB(1, 1), b3 + hstep); PG8_STAGE(PG8_SA(1, 0), a3, p0);
;             PG8_WAIT_V(8); PG8_WAIT_L(0); PG8_BAR; PG8_MMA(1, 0, At, B0); PG8_MMA(1, 1, At, B1); PG8_BAR; PG8_SCHED;
	s_add_i32 s6, s52, s21
	v_lshl_add_u64 v[216:217], v[212:213], 0, s[72:73]
	s_mov_b32 m0, s6
	ds_read_b128 v[178:181], v141 offset:49152
	ds_read_b128 v[182:185], v141 offset:50176
	ds_read_b128 v[186:189], v141 offset:51200
	ds_read_b128 v[190:193], v141 offset:52224
	ds_read_b128 v[194:197], v141 offset:53248
	ds_read_b128 v[198:201], v141 offset:54272
	ds_read_b128 v[202:205], v141 offset:55296
	ds_read_b128 v[206:209], v141 offset:56320
	global_load_lds_dwordx4 v[216:217], off
	v_lshl_add_u64 v[216:217], v[212:213], 0, s[86:87]
	s_add_i32 m0, s6, 0x2000
	s_add_i32 s6, s53, s21
	global_load_lds_dwordx4 v[216:217], off
	v_lshl_add_u64 v[216:217], v[212:213], 0, s[74:75]
	s_mov_b32 m0, s6
	v_lshl_add_u64 v[212:213], v[212:213], 0, s[88:89]
	global_load_lds_dwordx4 v[216:217], off
	s_add_i32 m0, s6, 0x2000
	v_lshl_add_u64 v[210:211], v[210:211], 0, s[72:73]
	global_load_lds_dwordx4 v[212:213], off
	v_lshl_add_u64 v[212:213], v[214:215], 0, s[72:73]
	s_mov_b32 m0, s57
	s_nop 0
	global_load_lds_dwordx4 v[212:213], off
	s_mov_b32 m0, s58
	s_nop 0
	global_load_lds_dwordx4 v[210:211], off
	s_waitcnt vmcnt(8)
	s_waitcnt lgkmcnt(0)
	s_barrier
	s_setprio 1
	s_waitcnt lgkmcnt(0)
	v_mfma_f32_16x16x32_bf16 v[60:63], v[146:149], v[178:181], v[60:63]
	v_mfma_f32_16x16x32_bf16 v[56:59], v[154:157], v[178:181], v[56:59]
	v_mfma_f32_16x16x32_bf16 v[52:55], v[146:149], v[186:189], v[52:55]
	v_mfma_f32_16x16x32_bf16 v[48:51], v[154:157], v[186:189], v[48:51]
	v_mfma_f32_16x16x32_bf16 v[20:23], v[146:149], v[194:197], v[20:23]
	v_mfma_f32_16x16x32_bf16 v[16:19], v[154:157], v[194:197], v[16:19]
	v_mfma_f32_16x16x32_bf16 v[4:7], v[146:149], v[202:205], v[4:7]
	v_mfma_f32_16x16x32_bf16 v[0:3], v[154:157], v[202:205], v[0:3]
	v_mfma_f32_16x16x32_bf16 v[60:63], v[150:153], v[182:185], v[60:63]
	v_mfma_f32_16x16x32_bf16 v[56:59], v[158:161], v[182:185], v[56:59]
	v_mfma_f32_16x16x32_bf16 v[52:55], v[150:153], v[190:193], v[52:55]
	v_mfma_f32_16x16x32_bf16 v[48:51], v[158:161], v[190:193], v[48:51]
	v_mfma_f32_16x16x32_bf16 v[20:23], v[150:153], v[198:201], v[20:23]
	v_mfma_f32_16x16x32_bf16 v[16:19], v[158:161], v[198:201], v[16:19]
	v_mfma_f32_16x16x32_bf16 v[4:7], v[150:153], v[206:209], v[4:7]
	v_mfma_f32_16x16x32_bf16 v[0:3], v[158:161], v[206:209], v[0:3]
	s_setprio 0
	s_setprio 1
	v_mfma_f32_16x16x32_bf16 v[44:47], v[162:165], v[178:181], v[44:47]
	v_mfma_f32_16x16x32_bf16 v[40:43], v[170:173], v[178:181], v[40:43]
	v_mfma_f32_16x16x32_bf16 v[36:39], v[162:165], v[186:189], v[36:39]
	v_mfma_f32_16x16x32_bf16 v[32:35], v[170:173], v[186:189], v[32:35]
	v_mfma_f32_16x16x32_bf16 v[24:27], v[162:165], v[194:197], v[24:27]
	v_mfma_f32_16x16x32_bf16 v[28:31], v[170:173], v[194:197], v[28:31]
	v_mfma_f32_16x16x32_bf16 v[8:11], v[162:165], v[202:205], v[8:11]
	v_mfma_f32_16x16x32_bf16 v[12:15], v[170:173], v[202:205], v[12:15]
	v_mfma_f32_16x16x32_bf16 v[44:47], v[166:169], v[182:185], v[44:47]
	v_mfma_f32_16x16x32_bf16 v[40:43], v[174:177], v[182:185], v[40:43]
	v_mfma_f32_16x16x32_bf16 v[36:39], v[166:169], v[190:193], v[36:39]
	v_mfma_f32_16x16x32_bf16 v[32:35], v[174:177], v[190:193], v[32:35]
	v_mfma_f32_16x16x32_bf16 v[24:27], v[166:169], v[198:201], v[24:27]
	v_mfma_f32_16x16x32_bf16 v[28:31], v[174:177], v[198:201], v[28:31]
	v_mfma_f32_16x16x32_bf16 v[8:11], v[166:169], v[206:209], v[8:11]
	v_mfma_f32_16x16x32_bf16 v[12:15], v[174:177], v[206:209], v[12:15]
	s_setprio 0
	s_barrier
	s_add_i32 s6, s68, 2
	s_cmp_gt_u32 s68, 5
	s_mov_b32 s68, s6
	s_cbranch_scc1 .LBB0_1676
